# sequence-DFT tile epilogue: the Nyquist-term loads reduced from 16 serialized (load, full wait) pairs to 4 loads issued together and one wait
# speedup vs baseline: 1.0058x; 1.0004x over previous
; template <bool I8 = false>
; __device__ __forceinline__ void gemm_mainloop(const bf16_t* __restrict__ A, int lda, const bf16_t* __restrict__ Bt, int ldb,
;                                               int K, int m0, int n0, f32x4 (&acc)[4][4], char* smem) {
;     ...
;   for (int kt = 0; kt < nk; ++kt) {
;     const int cur = kt & 1;
;     if (kt + 1 < nk) GSTAGE(cur ^ 1, kt + 1);
;     const char* sA = smem + cur * 32768;
;     const char* sB = sA + 16384;
; #pragma unroll
;     for (int kk = 0; kk < 2; ++kk) {
;       bf16x8 af[4], bfr[4];
;       const int ch = kk * 4 + (lane >> 4);
; #pragma unroll
;       for (int i = 0; i < 4; ++i) {
;         int row = wm * 64 + i * 16 + (lane & 15);
;         af[i] = *reinterpret_cast<const bf16x8*>(sA + row * 128 + ((ch ^ (row & 7)) << 4));
;         int col = wn * 64 + i * 16 + (lane & 15);
;         bfr[i] = *reinterpret_cast<const bf16x8*>(sB + col * 128 + ((ch ^ (col & 7)) << 4));
;       }
; #pragma unroll
;       for (int i = 0; i < 4; ++i)
; #pragma unroll
;         for (int j = 0; j < 4; ++j) {
;           if (I8) {
;             typedef __attribute__((ext_vector_type(4))) int i32x4;
;             acc[i][j] = __builtin_bit_cast(f32x4, __builtin_amdgcn_mfma_i32_16x16x64_i8(__builtin_bit_cast(i32x4, af[i]), __builtin_bit_cast(i32x4, bfr[j]),
;                                                                                          __builtin_bit_cast(i32x4, acc[i][j]), 0, 0, 0));
;           } else {
;             acc[i][j] = __builtin_amdgcn_mfma_f32_16x16x32_bf16(af[i], bfr[j], acc[i][j], 0, 0, 0);
;           }
;         }
;     }
;     asm volatile("s_waitcnt vmcnt(0)" ::: "memory");
;     __syncthreads();
;   }
.LBB0_771:
	s_and_b32 s63, s62, 0x8000
	s_xor_b32 s64, s63, 0x8000
	v_add_u32_e32 v220, s64, v202
	v_lshl_add_u64 v[204:205], v[180:181], 0, s[8:9]
	v_readfirstlane_b32 s64, v220
	v_add_u32_e32 v221, 0x4000, v220
	v_lshl_add_u64 v[206:207], v[178:179], 0, s[8:9]
	v_lshl_add_u64 v[208:209], v[204:205], 0, s[54:55]
	v_add_u32_e32 v222, 0x1000, v220
	v_readfirstlane_b32 s65, v221
	s_mov_b32 m0, s64
	v_lshl_add_u64 v[210:211], v[206:207], 0, s[54:55]
	v_add_u32_e32 v223, 0x5000, v220
	v_readfirstlane_b32 s68, v222
	global_load_lds_dwordx4 v[208:209], off
	s_mov_b32 m0, s65
	v_lshl_add_u64 v[212:213], v[204:205], 0, s[56:57]
	v_add_u32_e32 v224, 0x2000, v220
	v_readfirstlane_b32 s69, v223
	global_load_lds_dwordx4 v[210:211], off
	s_mov_b32 m0, s68
	v_lshl_add_u64 v[214:215], v[206:207], 0, s[56:57]
	v_add_u32_e32 v225, 0x6000, v220
	v_readfirstlane_b32 s70, v224
	global_load_lds_dwordx4 v[212:213], off
	s_mov_b32 m0, s69
	v_lshl_add_u64 v[216:217], v[204:205], 0, s[58:59]
	v_add_u32_e32 v226, 0x3000, v220
	v_readfirstlane_b32 s71, v225
	global_load_lds_dwordx4 v[214:215], off
	s_mov_b32 m0, s70
	v_lshl_add_u64 v[218:219], v[206:207], 0, s[58:59]
	v_add_u32_e32 v220, 0x7000, v220
	v_readfirstlane_b32 s72, v226
	global_load_lds_dwordx4 v[216:217], off
	s_mov_b32 m0, s71
	v_lshl_add_u64 v[204:205], v[204:205], 0, s[60:61]
	v_readfirstlane_b32 s73, v220
	global_load_lds_dwordx4 v[218:219], off
	s_mov_b32 m0, s72
	v_lshl_add_u64 v[206:207], v[206:207], 0, s[60:61]
	global_load_lds_dwordx4 v[204:205], off
	s_mov_b32 m0, s73
	v_or_b32_e32 v196, s63, v203
	global_load_lds_dwordx4 v[206:207], off
	v_add_u32_e32 v228, v196, v200
	v_add_u32_e32 v196, v196, v199
	ds_read_b128 v[204:207], v228
	ds_read_b128 v[208:211], v196 offset:16384
	ds_read_b128 v[212:215], v228 offset:2048
	ds_read_b128 v[216:219], v196 offset:18432
	ds_read_b128 v[220:223], v196 offset:20480
	ds_read_b128 v[224:227], v196 offset:22528
	s_waitcnt lgkmcnt(0)
	v_mfma_f32_16x16x32_bf16 v[174:177], v[204:207], v[208:211], v[174:177]
	v_or_b32_e32 v196, s63, v201
	s_add_i32 s62, s62, 0x8000
	s_add_u32 s8, s8, 0x80
	v_mfma_f32_16x16x32_bf16 v[170:173], v[204:207], v[216:219], v[170:173]
	s_addc_u32 s9, s9, 0
	s_cmpk_lg_i32 s8, 0x780
	v_mfma_f32_16x16x32_bf16 v[162:165], v[204:207], v[220:223], v[162:165]
	v_mfma_f32_16x16x32_bf16 v[158:161], v[204:207], v[224:227], v[158:161]
	v_mfma_f32_16x16x32_bf16 v[150:153], v[212:215], v[208:211], v[150:153]
	v_mfma_f32_16x16x32_bf16 v[146:149], v[212:215], v[216:219], v[146:149]
	v_mfma_f32_16x16x32_bf16 v[142:145], v[212:215], v[220:223], v[142:145]
	v_mfma_f32_16x16x32_bf16 v[138:141], v[212:215], v[224:227], v[138:141]
	ds_read_b128 v[204:207], v228 offset:4096
	ds_read_b128 v[212:215], v228 offset:6144
	v_add_u32_e32 v228, v196, v200
	v_add_u32_e32 v196, v196, v199
	s_waitcnt lgkmcnt(0)
	v_mfma_f32_16x16x32_bf16 v[134:137], v[204:207], v[208:211], v[134:137]
	v_mfma_f32_16x16x32_bf16 v[130:133], v[204:207], v[216:219], v[130:133]
	v_mfma_f32_16x16x32_bf16 v[126:129], v[204:207], v[220:223], v[126:129]
	v_mfma_f32_16x16x32_bf16 v[122:125], v[204:207], v[224:227], v[122:125]
	ds_read_b128 v[204:207], v228
	v_mfma_f32_16x16x32_bf16 v[118:121], v[212:215], v[208:211], v[118:121]
	v_mfma_f32_16x16x32_bf16 v[114:117], v[212:215], v[216:219], v[114:117]
	v_mfma_f32_16x16x32_bf16 v[166:169], v[212:215], v[220:223], v[166:169]
	v_mfma_f32_16x16x32_bf16 v[154:157], v[212:215], v[224:227], v[154:157]
	ds_read_b128 v[208:211], v196 offset:16384
	ds_read_b128 v[212:215], v228 offset:2048
	ds_read_b128 v[216:219], v196 offset:18432
	ds_read_b128 v[220:223], v196 offset:20480
	ds_read_b128 v[224:227], v196 offset:22528
	s_waitcnt lgkmcnt(0)
	v_mfma_f32_16x16x32_bf16 v[174:177], v[204:207], v[208:211], v[174:177]
	v_mfma_f32_16x16x32_bf16 v[170:173], v[204:207], v[216:219], v[170:173]
	v_mfma_f32_16x16x32_bf16 v[162:165], v[204:207], v[220:223], v[162:165]
	v_mfma_f32_16x16x32_bf16 v[158:161], v[204:207], v[224:227], v[158:161]
	v_mfma_f32_16x16x32_bf16 v[150:153], v[212:215], v[208:211], v[150:153]
	v_mfma_f32_16x16x32_bf16 v[146:149], v[212:215], v[216:219], v[146:149]
	v_mfma_f32_16x16x32_bf16 v[142:145], v[212:215], v[220:223], v[142:145]
	v_mfma_f32_16x16x32_bf16 v[138:141], v[212:215], v[224:227], v[138:141]
	ds_read_b128 v[204:207], v228 offset:4096
	ds_read_b128 v[212:215], v228 offset:6144
	s_waitcnt vmcnt(0)
	s_waitcnt vmcnt(0) lgkmcnt(0)
	v_mfma_f32_16x16x32_bf16 v[134:137], v[204:207], v[208:211], v[134:137]
	s_barrier
	v_mfma_f32_16x16x32_bf16 v[130:133], v[204:207], v[216:219], v[130:133]
	v_mfma_f32_16x16x32_bf16 v[126:129], v[204:207], v[220:223], v[126:129]
	v_mfma_f32_16x16x32_bf16 v[122:125], v[204:207], v[224:227], v[122:125]
	v_mfma_f32_16x16x32_bf16 v[118:121], v[212:215], v[208:211], v[118:121]
	v_mfma_f32_16x16x32_bf16 v[114:117], v[212:215], v[216:219], v[114:117]
	v_mfma_f32_16x16x32_bf16 v[166:169], v[212:215], v[220:223], v[166:169]
	v_mfma_f32_16x16x32_bf16 v[154:157], v[212:215], v[224:227], v[154:157]
	s_cbranch_scc1 .LBB0_771
; __device__ __forceinline__ float bf2f(bf16_t h) { return __uint_as_float(((uint32_t)h) << 16); }
; __device__ void phase_ssd_dft(KParams& p, int bid, int nb, char* smem) {
;     ...
;     gemm_mainloop(p.dftm, 2048, Fb, 2048, 1024, tm * 128, tn * 128, accC, smem);
;     gemm_mainloop(p.dftm + 1024, 2048, Fb + 1024, 2048, 1024, tm * 128, tn * 128, accS, smem);
;     const int lane = threadIdx.x & 63, w = threadIdx.x >> 6, wm = w >> 1, wn = w & 1;
; #pragma unroll
;     for (int i = 0; i < 4; ++i) {
;       int lq_ = lane >> 4, lr_ = lane & 15;
;       asm volatile("" : "+v"(lq_), "+v"(lr_));
; #pragma unroll
;       for (int j = 0; j < 4; ++j) {
;         const int k0 = tm * 128 + wm * 64 + i * 16 + lq_ * 4;
;         const int ch = tn * 128 + wn * 64 + j * 16 + lr_;
;         const float a = bf2f(p.ABt[((size_t)b * 1024 + ch) * 4096 + 1024]);
; #pragma unroll
;         for (int r = 0; r < 4; ++r) {
;           const int k = k0 + r;
;           const float as = (k & 1) ? -a : a;
;           const float c = accC[i][j][r], sn = accS[i][j][r];
;           p.ycat[((size_t)b * L + k) * D + ch] = f2bf(c - sn + as);
;           if (k > 0) p.ycat[((size_t)b * L + (L - k)) * D + ch] = f2bf(c + sn + as);
;         }
	v_mfma_f32_16x16x32_bf16 v[34:37], v[86:89], v[94:97], v[34:37]
	s_lshl_b64 s[8:9], s[6:7], 23
	s_add_u32 s64, s10, s8
	s_addc_u32 s65, s11, s9
	v_mfma_f32_16x16x32_bf16 v[26:29], v[86:89], v[70:73], v[26:29]
	s_lshl_b64 s[62:63], s[6:7], 11
	v_mfma_f32_16x16x32_bf16 v[42:45], v[58:61], v[94:97], v[42:45]
	v_mfma_f32_16x16x32_bf16 v[38:41], v[58:61], v[70:73], v[38:41]
	v_mfma_f32_16x16x32_bf16 v[22:25], v[82:85], v[94:97], v[22:25]
	v_mfma_f32_16x16x32_bf16 v[18:21], v[82:85], v[70:73], v[18:21]
	v_mfma_f32_16x16x32_bf16 v[10:13], v[74:77], v[94:97], v[10:13]
	v_mfma_f32_16x16x32_bf16 v[50:53], v[74:77], v[70:73], v[50:53]
	v_add_u32_e32 v70, v203, v199
	v_mfma_f32_16x16x32_bf16 v[94:97], v[106:109], v[102:105], v[34:37]
	v_mfma_f32_16x16x32_bf16 v[74:77], v[106:109], v[54:57], v[26:29]
	v_add_u32_e32 v106, v203, v200
	ds_read_b128 v[82:85], v106 offset:34816
	v_mfma_f32_16x16x32_bf16 v[178:181], v[110:113], v[102:105], v[42:45]
	ds_read_b128 v[26:29], v70 offset:49152
	v_mfma_f32_16x16x32_bf16 v[110:113], v[110:113], v[54:57], v[38:41]
	v_mfma_f32_16x16x32_bf16 v[58:61], v[98:101], v[102:105], v[22:25]
	s_nop 1
	ds_read_b128 v[38:41], v70 offset:51200
	v_mfma_f32_16x16x32_bf16 v[42:45], v[98:101], v[54:57], v[18:21]
	v_mfma_f32_16x16x32_bf16 v[22:25], v[66:69], v[102:105], v[10:13]
	s_nop 1
	ds_read_b128 v[18:21], v106 offset:32768
	ds_read_b128 v[102:105], v106 offset:36864
	v_mfma_f32_16x16x32_bf16 v[10:13], v[66:69], v[54:57], v[50:53]
	ds_read_b128 v[54:57], v70 offset:53248
	ds_read_b128 v[70:73], v70 offset:55296
	s_waitcnt lgkmcnt(5)
	v_mfma_f32_16x16x32_bf16 v[86:89], v[82:85], v[26:29], v[150:153]
	s_waitcnt lgkmcnt(4)
	v_mfma_f32_16x16x32_bf16 v[98:101], v[82:85], v[38:41], v[146:149]
	s_waitcnt lgkmcnt(1)
	v_mfma_f32_16x16x32_bf16 v[142:145], v[82:85], v[54:57], v[142:145]
	s_waitcnt lgkmcnt(0)
	v_mfma_f32_16x16x32_bf16 v[82:85], v[82:85], v[70:73], v[138:141]
	v_mfma_f32_16x16x32_bf16 v[134:137], v[102:105], v[26:29], v[134:137]
	v_mfma_f32_16x16x32_bf16 v[130:133], v[102:105], v[38:41], v[130:133]
	v_mfma_f32_16x16x32_bf16 v[138:141], v[102:105], v[54:57], v[126:129]
	v_mfma_f32_16x16x32_bf16 v[146:149], v[102:105], v[70:73], v[122:125]
	ds_read_b128 v[102:105], v106 offset:38912
	s_nop 0
	v_add_u32_e32 v126, v201, v200
	v_mfma_f32_16x16x32_bf16 v[50:53], v[18:21], v[38:41], v[170:173]
	s_waitcnt lgkmcnt(0)
	v_mfma_f32_16x16x32_bf16 v[150:153], v[102:105], v[38:41], v[114:117]
	ds_read_b128 v[38:41], v126 offset:32768
	v_mfma_f32_16x16x32_bf16 v[34:37], v[18:21], v[26:29], v[174:177]
	v_mfma_f32_16x16x32_bf16 v[66:69], v[18:21], v[54:57], v[162:165]
	v_mfma_f32_16x16x32_bf16 v[18:21], v[18:21], v[70:73], v[158:161]
	v_mfma_f32_16x16x32_bf16 v[158:161], v[102:105], v[54:57], v[166:169]
	v_add_u32_e32 v54, v201, v199
	ds_read_b128 v[162:165], v54 offset:49152
	ds_read_b128 v[170:173], v54 offset:55296
	ds_read_b128 v[166:169], v54 offset:53248
	s_waitcnt lgkmcnt(2)
	v_mfma_f32_16x16x32_bf16 v[122:125], v[38:41], v[162:165], v[34:37]
	s_nop 2
	ds_read_b128 v[34:37], v54 offset:51200
	s_waitcnt lgkmcnt(2)
	v_mfma_f32_16x16x32_bf16 v[106:109], v[38:41], v[170:173], v[18:21]
	s_nop 2
	ds_read_b128 v[18:21], v126 offset:34816
	v_mfma_f32_16x16x32_bf16 v[26:29], v[102:105], v[26:29], v[118:121]
	v_mfma_f32_16x16x32_bf16 v[154:157], v[102:105], v[70:73], v[154:157]
	s_waitcnt lgkmcnt(0)
	v_mfma_f32_16x16x32_bf16 v[102:105], v[18:21], v[162:165], v[86:89]
	v_mfma_f32_16x16x32_bf16 v[98:101], v[18:21], v[34:37], v[98:101]
	v_mfma_f32_16x16x32_bf16 v[86:89], v[18:21], v[166:169], v[142:145]
	s_nop 2
	v_or_b32_e32 v142, s67, v189
	v_mfma_f32_16x16x32_bf16 v[82:85], v[18:21], v[170:173], v[82:85]
	v_mov_b32_e32 v18, v185
	v_mov_b32_e32 v20, v195
	v_add_u32_e32 v143, s66, v193
	v_mfma_f32_16x16x32_bf16 v[118:121], v[38:41], v[34:37], v[50:53]
	v_mfma_f32_16x16x32_bf16 v[114:117], v[38:41], v[166:169], v[66:69]
	ds_read_b128 v[174:177], v126 offset:38912
	ds_read_b128 v[38:41], v126 offset:36864
	s_waitcnt vmcnt(0)
	s_waitcnt lgkmcnt(0)
	s_barrier
	v_mfma_f32_16x16x32_bf16 v[70:73], v[38:41], v[162:165], v[134:137]
	v_add_u32_e32 v128, v18, v142
	v_ashrrev_i32_e32 v129, 31, v128
	v_lshlrev_b64 v[18:19], 13, v[128:129]
	v_lshl_add_u64 v[18:19], s[64:65], 0, v[18:19]
	global_load_ushort v18, v[18:19], off offset:2048
	v_add_u32_e32 v234, 16, v128
	v_ashrrev_i32_e32 v235, 31, v234
	v_lshlrev_b64 v[234:235], 13, v[234:235]
	v_lshl_add_u64 v[234:235], s[64:65], 0, v[234:235]
	global_load_ushort v230, v[234:235], off offset:2048
	v_add_u32_e32 v236, 32, v128
	v_ashrrev_i32_e32 v237, 31, v236
	v_lshlrev_b64 v[236:237], 13, v[236:237]
	v_lshl_add_u64 v[236:237], s[64:65], 0, v[236:237]
	global_load_ushort v231, v[236:237], off offset:2048
	v_add_u32_e32 v238, 48, v128
	v_ashrrev_i32_e32 v239, 31, v238
	v_lshlrev_b64 v[238:239], 13, v[238:239]
	v_lshl_add_u64 v[238:239], s[64:65], 0, v[238:239]
	global_load_ushort v232, v[238:239], off offset:2048
	v_lshl_add_u32 v136, v20, 2, v143
	v_ashrrev_i32_e32 v137, 31, v136
	v_mfma_f32_16x16x32_bf16 v[54:57], v[38:41], v[166:169], v[138:141]
	v_cmp_lt_i32_e64 s[6:7], 0, v136
	s_waitcnt vmcnt(0)
	v_mov_b32_e32 v229, v18
	v_lshlrev_b32_e32 v144, 16, v18
	v_sub_f32_e32 v18, v90, v122
	v_add_f32_e32 v18, v18, v144
	v_cvt_pk_bf16_f32 v20, v18, s0
	v_lshl_add_u64 v[18:19], s[62:63], 0, v[136:137]
	v_lshl_add_u64 v[140:141], v[128:129], 1, s[16:17]
	v_lshlrev_b64 v[134:135], 12, v[18:19]
	v_lshl_add_u64 v[18:19], v[140:141], 0, v[134:135]
	v_mfma_f32_16x16x32_bf16 v[66:69], v[38:41], v[34:37], v[130:133]
	global_store_short v[18:19], v20, off
	v_mfma_f32_16x16x32_bf16 v[50:53], v[38:41], v[170:173], v[146:149]
	s_nop 0
	v_sub_u32_e32 v130, 0x800, v136
	v_ashrrev_i32_e32 v131, 31, v130
	v_mfma_f32_16x16x32_bf16 v[38:41], v[174:177], v[162:165], v[26:29]
	v_mfma_f32_16x16x32_bf16 v[34:37], v[174:177], v[34:37], v[150:153]
	v_mfma_f32_16x16x32_bf16 v[26:29], v[174:177], v[166:169], v[158:161]
	v_mfma_f32_16x16x32_bf16 v[18:21], v[174:177], v[170:173], v[154:157]
	s_and_saveexec_b64 s[8:9], s[6:7]
	s_cbranch_execz .LBB0_774
	v_add_f32_e32 v90, v90, v122
	v_lshl_add_u64 v[126:127], s[62:63], 0, v[130:131]
	v_add_f32_e32 v90, v90, v144
	v_lshlrev_b64 v[126:127], 12, v[126:127]
	v_cvt_pk_bf16_f32 v90, v90, s0
	v_lshl_add_u64 v[126:127], v[140:141], 0, v[126:127]
	global_store_short v[126:127], v90, off

; __device__ __forceinline__ float bf2f(bf16_t h) { return __uint_as_float(((uint32_t)h) << 16); }
; __device__ void phase_ssd_dft(KParams& p, int bid, int nb, char* smem) {
;     ...
;         const int k0 = tm * 128 + wm * 64 + i * 16 + lq_ * 4;
;         const int ch = tn * 128 + wn * 64 + j * 16 + lr_;
;         const float a = bf2f(p.ABt[((size_t)b * 1024 + ch) * 4096 + 1024]);
; #pragma unroll
;         for (int r = 0; r < 4; ++r) {
;           const int k = k0 + r;
;           const float as = (k & 1) ? -a : a;
;           const float c = accC[i][j][r], sn = accS[i][j][r];
;           p.ycat[((size_t)b * L + k) * D + ch] = f2bf(c - sn + as);
;           if (k > 0) p.ycat[((size_t)b * L + (L - k)) * D + ch] = f2bf(c + sn + as);
.LBB0_780:
	s_or_b64 exec, exec, s[66:67]
	v_add_u32_e32 v92, 16, v128
	v_ashrrev_i32_e32 v93, 31, v92
	v_lshlrev_b64 v[124:125], 13, v[92:93]
	v_lshl_add_u64 v[124:125], s[64:65], 0, v[124:125]
	v_mov_b32_e32 v124, v230
	v_sub_f32_e32 v125, v178, v118
	v_lshl_add_u64 v[92:93], v[92:93], 1, s[16:17]
	v_lshlrev_b32_e32 v129, 16, v124
	v_add_f32_e32 v124, v125, v129
	v_cvt_pk_bf16_f32 v140, v124, s0
	v_lshl_add_u64 v[124:125], v[92:93], 0, v[134:135]
	global_store_short v[124:125], v140, off
	s_and_saveexec_b64 s[66:67], s[6:7]
	s_cbranch_execz .LBB0_782
	v_add_f32_e32 v118, v178, v118
	v_lshl_add_u64 v[124:125], s[62:63], 0, v[130:131]
	v_add_f32_e32 v118, v118, v129
	v_lshlrev_b64 v[124:125], 12, v[124:125]
	v_cvt_pk_bf16_f32 v118, v118, s0
	v_lshl_add_u64 v[124:125], v[92:93], 0, v[124:125]
	global_store_short v[124:125], v118, off

; __device__ __forceinline__ float bf2f(bf16_t h) { return __uint_as_float(((uint32_t)h) << 16); }
; __device__ void phase_ssd_dft(KParams& p, int bid, int nb, char* smem) {
;     ...
;         const int k0 = tm * 128 + wm * 64 + i * 16 + lq_ * 4;
;         const int ch = tn * 128 + wn * 64 + j * 16 + lr_;
;         const float a = bf2f(p.ABt[((size_t)b * 1024 + ch) * 4096 + 1024]);
; #pragma unroll
;         for (int r = 0; r < 4; ++r) {
;           const int k = k0 + r;
;           const float as = (k & 1) ? -a : a;
;           const float c = accC[i][j][r], sn = accS[i][j][r];
;           p.ycat[((size_t)b * L + k) * D + ch] = f2bf(c - sn + as);
;           if (k > 0) p.ycat[((size_t)b * L + (L - k)) * D + ch] = f2bf(c + sn + as);
.LBB0_786:
	s_or_b64 exec, exec, s[66:67]
	v_add_u32_e32 v92, 32, v128
	v_ashrrev_i32_e32 v93, 31, v92
	v_lshlrev_b64 v[118:119], 13, v[92:93]
	v_lshl_add_u64 v[118:119], s[64:65], 0, v[118:119]
	v_mov_b32_e32 v118, v231
	v_sub_f32_e32 v119, v78, v114
	v_lshl_add_u64 v[92:93], v[92:93], 1, s[16:17]
	v_lshlrev_b32_e32 v120, 16, v118
	v_add_f32_e32 v118, v119, v120
	v_cvt_pk_bf16_f32 v121, v118, s0
	v_lshl_add_u64 v[118:119], v[92:93], 0, v[134:135]
	global_store_short v[118:119], v121, off
	s_and_saveexec_b64 s[66:67], s[6:7]
	s_cbranch_execz .LBB0_788
	v_add_f32_e32 v78, v78, v114
	v_lshl_add_u64 v[118:119], s[62:63], 0, v[130:131]
	v_add_f32_e32 v78, v78, v120
	v_lshlrev_b64 v[118:119], 12, v[118:119]
	v_cvt_pk_bf16_f32 v78, v78, s0
	v_lshl_add_u64 v[118:119], v[92:93], 0, v[118:119]
	global_store_short v[118:119], v78, off

; __device__ __forceinline__ float bf2f(bf16_t h) { return __uint_as_float(((uint32_t)h) << 16); }
; __device__ void phase_ssd_dft(KParams& p, int bid, int nb, char* smem) {
;     ...
;         const int k0 = tm * 128 + wm * 64 + i * 16 + lq_ * 4;
;         const int ch = tn * 128 + wn * 64 + j * 16 + lr_;
;         const float a = bf2f(p.ABt[((size_t)b * 1024 + ch) * 4096 + 1024]);
; #pragma unroll
;         for (int r = 0; r < 4; ++r) {
;           const int k = k0 + r;
;           const float as = (k & 1) ? -a : a;
;           const float c = accC[i][j][r], sn = accS[i][j][r];
;           p.ycat[((size_t)b * L + k) * D + ch] = f2bf(c - sn + as);
;           if (k > 0) p.ycat[((size_t)b * L + (L - k)) * D + ch] = f2bf(c + sn + as);
.LBB0_792:
	s_or_b64 exec, exec, s[66:67]
	v_add_u32_e32 v78, 48, v128
	v_ashrrev_i32_e32 v79, 31, v78
	v_lshlrev_b64 v[80:81], 13, v[78:79]
	v_lshl_add_u64 v[80:81], s[64:65], 0, v[80:81]
	v_mov_b32_e32 v80, v232
	v_sub_f32_e32 v81, v110, v106
	v_lshl_add_u64 v[78:79], v[78:79], 1, s[16:17]
	v_lshl_add_u64 v[92:93], v[78:79], 0, v[134:135]
	v_lshlrev_b32_e32 v80, 16, v80
	v_add_f32_e32 v81, v81, v80
	v_cvt_pk_bf16_f32 v81, v81, s0
	global_store_short v[92:93], v81, off
	s_and_saveexec_b64 s[66:67], s[6:7]
	s_cbranch_execz .LBB0_794
	v_add_f32_e32 v81, v110, v106
	v_lshl_add_u64 v[92:93], s[62:63], 0, v[130:131]
	v_add_f32_e32 v81, v81, v80
	v_lshlrev_b64 v[92:93], 12, v[92:93]
	v_cvt_pk_bf16_f32 v81, v81, s0
	v_lshl_add_u64 v[92:93], v[78:79], 0, v[92:93]
	global_store_short v[92:93], v81, off

; __device__ __forceinline__ float bf2f(bf16_t h) { return __uint_as_float(((uint32_t)h) << 16); }
; __device__ void phase_ssd_dft(KParams& p, int bid, int nb, char* smem) {
;     ...
;         const int k0 = tm * 128 + wm * 64 + i * 16 + lq_ * 4;
;         const int ch = tn * 128 + wn * 64 + j * 16 + lr_;
;         const float a = bf2f(p.ABt[((size_t)b * 1024 + ch) * 4096 + 1024]);
; #pragma unroll
;         for (int r = 0; r < 4; ++r) {
;           const int k = k0 + r;
;           const float as = (k & 1) ? -a : a;
;           const float c = accC[i][j][r], sn = accS[i][j][r];
;           p.ycat[((size_t)b * L + k) * D + ch] = f2bf(c - sn + as);
;           if (k > 0) p.ycat[((size_t)b * L + (L - k)) * D + ch] = f2bf(c + sn + as);
.LBB0_800:
	s_or_b64 exec, exec, s[6:7]
	v_mov_b32_e32 v78, v185
	v_mov_b32_e32 v80, v195
	v_sub_f32_e32 v108, v62, v102
	v_add_u32_e32 v90, v78, v142
	v_ashrrev_i32_e32 v91, 31, v90
	v_lshlrev_b64 v[78:79], 13, v[90:91]
	v_lshl_add_u64 v[78:79], s[64:65], 0, v[78:79]
	v_mov_b32_e32 v81, v229
	v_lshlrev_b32_e32 v78, 2, v80
	v_add3_u32 v92, v78, v143, 16
	v_ashrrev_i32_e32 v93, 31, v92
	v_lshl_add_u64 v[112:113], v[90:91], 1, s[16:17]
	v_lshl_add_u64 v[78:79], s[62:63], 0, v[92:93]
	v_lshlrev_b64 v[106:107], 12, v[78:79]
	v_sub_u32_e32 v80, 0x800, v92
	v_lshl_add_u64 v[78:79], v[112:113], 0, v[106:107]
	v_cmp_lt_i32_e64 s[6:7], 0, v92
	v_lshlrev_b32_e32 v91, 16, v81
	v_add_f32_e32 v81, v108, v91
	v_cvt_pk_bf16_f32 v81, v81, s0
	global_store_short v[78:79], v81, off
	v_ashrrev_i32_e32 v81, 31, v80
	s_and_saveexec_b64 s[8:9], s[6:7]
	s_cbranch_execz .LBB0_802
	v_add_f32_e32 v62, v62, v102
	v_lshl_add_u64 v[78:79], s[62:63], 0, v[80:81]
	v_add_f32_e32 v62, v62, v91
	v_lshlrev_b64 v[78:79], 12, v[78:79]
	v_cvt_pk_bf16_f32 v62, v62, s0
	v_lshl_add_u64 v[78:79], v[112:113], 0, v[78:79]
	global_store_short v[78:79], v62, off

; __device__ __forceinline__ float bf2f(bf16_t h) { return __uint_as_float(((uint32_t)h) << 16); }
; __device__ void phase_ssd_dft(KParams& p, int bid, int nb, char* smem) {
;     ...
;         const int k0 = tm * 128 + wm * 64 + i * 16 + lq_ * 4;
;         const int ch = tn * 128 + wn * 64 + j * 16 + lr_;
;         const float a = bf2f(p.ABt[((size_t)b * 1024 + ch) * 4096 + 1024]);
; #pragma unroll
;         for (int r = 0; r < 4; ++r) {
;           const int k = k0 + r;
;           const float as = (k & 1) ? -a : a;
;           const float c = accC[i][j][r], sn = accS[i][j][r];
;           p.ycat[((size_t)b * L + k) * D + ch] = f2bf(c - sn + as);
;           if (k > 0) p.ycat[((size_t)b * L + (L - k)) * D + ch] = f2bf(c + sn + as);
.LBB0_808:
	s_or_b64 exec, exec, s[66:67]
	v_add_u32_e32 v64, 16, v90
	v_ashrrev_i32_e32 v65, 31, v64
	v_lshlrev_b64 v[104:105], 13, v[64:65]
	v_lshl_add_u64 v[104:105], s[64:65], 0, v[104:105]
	v_mov_b32_e32 v91, v230
	v_sub_f32_e32 v104, v94, v98
	v_lshl_add_u64 v[64:65], v[64:65], 1, s[16:17]
	v_lshlrev_b32_e32 v91, 16, v91
	v_add_f32_e32 v104, v104, v91
	v_cvt_pk_bf16_f32 v112, v104, s0
	v_lshl_add_u64 v[104:105], v[64:65], 0, v[106:107]
	global_store_short v[104:105], v112, off
	s_and_saveexec_b64 s[66:67], s[6:7]
	s_cbranch_execz .LBB0_810
	v_add_f32_e32 v94, v94, v98
	v_lshl_add_u64 v[104:105], s[62:63], 0, v[80:81]
	v_add_f32_e32 v94, v94, v91
	v_lshlrev_b64 v[104:105], 12, v[104:105]
	v_cvt_pk_bf16_f32 v94, v94, s0
	v_lshl_add_u64 v[104:105], v[64:65], 0, v[104:105]
	global_store_short v[104:105], v94, off

; __device__ __forceinline__ float bf2f(bf16_t h) { return __uint_as_float(((uint32_t)h) << 16); }
; __device__ void phase_ssd_dft(KParams& p, int bid, int nb, char* smem) {
;     ...
;         const int k0 = tm * 128 + wm * 64 + i * 16 + lq_ * 4;
;         const int ch = tn * 128 + wn * 64 + j * 16 + lr_;
;         const float a = bf2f(p.ABt[((size_t)b * 1024 + ch) * 4096 + 1024]);
; #pragma unroll
;         for (int r = 0; r < 4; ++r) {
;           const int k = k0 + r;
;           const float as = (k & 1) ? -a : a;
;           const float c = accC[i][j][r], sn = accS[i][j][r];
;           p.ycat[((size_t)b * L + k) * D + ch] = f2bf(c - sn + as);
;           if (k > 0) p.ycat[((size_t)b * L + (L - k)) * D + ch] = f2bf(c + sn + as);
.LBB0_814:
	s_or_b64 exec, exec, s[66:67]
	v_add_u32_e32 v64, 32, v90
	v_ashrrev_i32_e32 v65, 31, v64
	v_lshlrev_b64 v[94:95], 13, v[64:65]
	v_lshl_add_u64 v[94:95], s[64:65], 0, v[94:95]
	v_mov_b32_e32 v91, v231
	v_sub_f32_e32 v94, v46, v86
	v_lshl_add_u64 v[64:65], v[64:65], 1, s[16:17]
	v_lshlrev_b32_e32 v91, 16, v91
	v_add_f32_e32 v94, v94, v91
	v_cvt_pk_bf16_f32 v96, v94, s0
	v_lshl_add_u64 v[94:95], v[64:65], 0, v[106:107]
	global_store_short v[94:95], v96, off
	s_and_saveexec_b64 s[66:67], s[6:7]
	s_cbranch_execz .LBB0_816
	v_add_f32_e32 v46, v46, v86
	v_lshl_add_u64 v[94:95], s[62:63], 0, v[80:81]
	v_add_f32_e32 v46, v46, v91
	v_lshlrev_b64 v[94:95], 12, v[94:95]
	v_cvt_pk_bf16_f32 v46, v46, s0
	v_lshl_add_u64 v[94:95], v[64:65], 0, v[94:95]
	global_store_short v[94:95], v46, off

; __device__ __forceinline__ float bf2f(bf16_t h) { return __uint_as_float(((uint32_t)h) << 16); }
; __device__ void phase_ssd_dft(KParams& p, int bid, int nb, char* smem) {
;     ...
;         const int k0 = tm * 128 + wm * 64 + i * 16 + lq_ * 4;
;         const int ch = tn * 128 + wn * 64 + j * 16 + lr_;
;         const float a = bf2f(p.ABt[((size_t)b * 1024 + ch) * 4096 + 1024]);
; #pragma unroll
;         for (int r = 0; r < 4; ++r) {
;           const int k = k0 + r;
;           const float as = (k & 1) ? -a : a;
;           const float c = accC[i][j][r], sn = accS[i][j][r];
;           p.ycat[((size_t)b * L + k) * D + ch] = f2bf(c - sn + as);
;           if (k > 0) p.ycat[((size_t)b * L + (L - k)) * D + ch] = f2bf(c + sn + as);
.LBB0_820:
	s_or_b64 exec, exec, s[66:67]
	v_add_u32_e32 v46, 48, v90
	v_ashrrev_i32_e32 v47, 31, v46
	v_lshlrev_b64 v[48:49], 13, v[46:47]
	v_lshl_add_u64 v[48:49], s[64:65], 0, v[48:49]
	v_mov_b32_e32 v48, v232
	v_sub_f32_e32 v49, v74, v82
	v_lshl_add_u64 v[46:47], v[46:47], 1, s[16:17]
	v_lshl_add_u64 v[64:65], v[46:47], 0, v[106:107]
	v_lshlrev_b32_e32 v48, 16, v48
	v_add_f32_e32 v49, v49, v48
	v_cvt_pk_bf16_f32 v49, v49, s0
	global_store_short v[64:65], v49, off
	s_and_saveexec_b64 s[66:67], s[6:7]
	s_cbranch_execz .LBB0_822
	v_add_f32_e32 v49, v74, v82
	v_lshl_add_u64 v[64:65], s[62:63], 0, v[80:81]
	v_add_f32_e32 v49, v49, v48
	v_lshlrev_b64 v[64:65], 12, v[64:65]
	v_cvt_pk_bf16_f32 v49, v49, s0
	v_lshl_add_u64 v[64:65], v[46:47], 0, v[64:65]
	global_store_short v[64:65], v49, off

; __device__ __forceinline__ float bf2f(bf16_t h) { return __uint_as_float(((uint32_t)h) << 16); }
; __device__ void phase_ssd_dft(KParams& p, int bid, int nb, char* smem) {
;     ...
;         const int k0 = tm * 128 + wm * 64 + i * 16 + lq_ * 4;
;         const int ch = tn * 128 + wn * 64 + j * 16 + lr_;
;         const float a = bf2f(p.ABt[((size_t)b * 1024 + ch) * 4096 + 1024]);
; #pragma unroll
;         for (int r = 0; r < 4; ++r) {
;           const int k = k0 + r;
;           const float as = (k & 1) ? -a : a;
;           const float c = accC[i][j][r], sn = accS[i][j][r];
;           p.ycat[((size_t)b * L + k) * D + ch] = f2bf(c - sn + as);
;           if (k > 0) p.ycat[((size_t)b * L + (L - k)) * D + ch] = f2bf(c + sn + as);
.LBB0_828:
	s_or_b64 exec, exec, s[6:7]
	v_mov_b32_e32 v48, v195
	v_mov_b32_e32 v46, v185
	v_sub_f32_e32 v76, v30, v70
	v_add_u32_e32 v62, v46, v142
	v_ashrrev_i32_e32 v63, 31, v62
	v_lshlrev_b64 v[46:47], 13, v[62:63]
	v_lshl_add_u64 v[46:47], s[64:65], 0, v[46:47]
	v_mov_b32_e32 v49, v229
	v_lshlrev_b32_e32 v46, 2, v48
	v_add3_u32 v64, v46, v143, 32
	v_ashrrev_i32_e32 v65, 31, v64
	v_lshl_add_u64 v[80:81], v[62:63], 1, s[16:17]
	v_lshl_add_u64 v[46:47], s[62:63], 0, v[64:65]
	v_lshlrev_b64 v[74:75], 12, v[46:47]
	v_sub_u32_e32 v48, 0x800, v64
	v_lshl_add_u64 v[46:47], v[80:81], 0, v[74:75]
	v_cmp_lt_i32_e64 s[6:7], 0, v64
	v_lshlrev_b32_e32 v63, 16, v49
	v_add_f32_e32 v49, v76, v63
	v_cvt_pk_bf16_f32 v49, v49, s0
	global_store_short v[46:47], v49, off
	v_ashrrev_i32_e32 v49, 31, v48
	s_and_saveexec_b64 s[8:9], s[6:7]
	s_cbranch_execz .LBB0_830
	v_add_f32_e32 v30, v30, v70
	v_lshl_add_u64 v[46:47], s[62:63], 0, v[48:49]
	v_add_f32_e32 v30, v30, v63
	v_lshlrev_b64 v[46:47], 12, v[46:47]
	v_cvt_pk_bf16_f32 v30, v30, s0
	v_lshl_add_u64 v[46:47], v[80:81], 0, v[46:47]
	global_store_short v[46:47], v30, off

; __device__ __forceinline__ float bf2f(bf16_t h) { return __uint_as_float(((uint32_t)h) << 16); }
; __device__ void phase_ssd_dft(KParams& p, int bid, int nb, char* smem) {
;     ...
;         const int k0 = tm * 128 + wm * 64 + i * 16 + lq_ * 4;
;         const int ch = tn * 128 + wn * 64 + j * 16 + lr_;
;         const float a = bf2f(p.ABt[((size_t)b * 1024 + ch) * 4096 + 1024]);
; #pragma unroll
;         for (int r = 0; r < 4; ++r) {
;           const int k = k0 + r;
;           const float as = (k & 1) ? -a : a;
;           const float c = accC[i][j][r], sn = accS[i][j][r];
;           p.ycat[((size_t)b * L + k) * D + ch] = f2bf(c - sn + as);
;           if (k > 0) p.ycat[((size_t)b * L + (L - k)) * D + ch] = f2bf(c + sn + as);
.LBB0_836:
	s_or_b64 exec, exec, s[66:67]
	v_add_u32_e32 v32, 16, v62
	v_ashrrev_i32_e32 v33, 31, v32
	v_lshlrev_b64 v[72:73], 13, v[32:33]
	v_lshl_add_u64 v[72:73], s[64:65], 0, v[72:73]
	v_mov_b32_e32 v63, v230
	v_sub_f32_e32 v72, v58, v66
	v_lshl_add_u64 v[32:33], v[32:33], 1, s[16:17]
	v_lshlrev_b32_e32 v63, 16, v63
	v_add_f32_e32 v72, v72, v63
	v_cvt_pk_bf16_f32 v80, v72, s0
	v_lshl_add_u64 v[72:73], v[32:33], 0, v[74:75]
	global_store_short v[72:73], v80, off
	s_and_saveexec_b64 s[66:67], s[6:7]
	s_cbranch_execz .LBB0_838
	v_add_f32_e32 v58, v58, v66
	v_lshl_add_u64 v[72:73], s[62:63], 0, v[48:49]
	v_add_f32_e32 v58, v58, v63
	v_lshlrev_b64 v[72:73], 12, v[72:73]
	v_cvt_pk_bf16_f32 v58, v58, s0
	v_lshl_add_u64 v[72:73], v[32:33], 0, v[72:73]
	global_store_short v[72:73], v58, off

; __device__ __forceinline__ float bf2f(bf16_t h) { return __uint_as_float(((uint32_t)h) << 16); }
; __device__ void phase_ssd_dft(KParams& p, int bid, int nb, char* smem) {
;     ...
;         const int k0 = tm * 128 + wm * 64 + i * 16 + lq_ * 4;
;         const int ch = tn * 128 + wn * 64 + j * 16 + lr_;
;         const float a = bf2f(p.ABt[((size_t)b * 1024 + ch) * 4096 + 1024]);
; #pragma unroll
;         for (int r = 0; r < 4; ++r) {
;           const int k = k0 + r;
;           const float as = (k & 1) ? -a : a;
;           const float c = accC[i][j][r], sn = accS[i][j][r];
;           p.ycat[((size_t)b * L + k) * D + ch] = f2bf(c - sn + as);
;           if (k > 0) p.ycat[((size_t)b * L + (L - k)) * D + ch] = f2bf(c + sn + as);
.LBB0_842:
	s_or_b64 exec, exec, s[66:67]
	v_add_u32_e32 v32, 32, v62
	v_ashrrev_i32_e32 v33, 31, v32
	v_lshlrev_b64 v[58:59], 13, v[32:33]
	v_lshl_add_u64 v[58:59], s[64:65], 0, v[58:59]
	v_mov_b32_e32 v58, v231
	v_sub_f32_e32 v59, v14, v54
	v_lshl_add_u64 v[32:33], v[32:33], 1, s[16:17]
	v_lshlrev_b32_e32 v60, 16, v58
	v_add_f32_e32 v58, v59, v60
	v_cvt_pk_bf16_f32 v61, v58, s0
	v_lshl_add_u64 v[58:59], v[32:33], 0, v[74:75]
	global_store_short v[58:59], v61, off
	s_and_saveexec_b64 s[66:67], s[6:7]
	s_cbranch_execz .LBB0_844
	v_add_f32_e32 v14, v14, v54
	v_lshl_add_u64 v[58:59], s[62:63], 0, v[48:49]
	v_add_f32_e32 v14, v14, v60
	v_lshlrev_b64 v[58:59], 12, v[58:59]
	v_cvt_pk_bf16_f32 v14, v14, s0
	v_lshl_add_u64 v[58:59], v[32:33], 0, v[58:59]
	global_store_short v[58:59], v14, off

; __device__ __forceinline__ float bf2f(bf16_t h) { return __uint_as_float(((uint32_t)h) << 16); }
; __device__ void phase_ssd_dft(KParams& p, int bid, int nb, char* smem) {
;     ...
;         const int k0 = tm * 128 + wm * 64 + i * 16 + lq_ * 4;
;         const int ch = tn * 128 + wn * 64 + j * 16 + lr_;
;         const float a = bf2f(p.ABt[((size_t)b * 1024 + ch) * 4096 + 1024]);
; #pragma unroll
;         for (int r = 0; r < 4; ++r) {
;           const int k = k0 + r;
;           const float as = (k & 1) ? -a : a;
;           const float c = accC[i][j][r], sn = accS[i][j][r];
;           p.ycat[((size_t)b * L + k) * D + ch] = f2bf(c - sn + as);
;           if (k > 0) p.ycat[((size_t)b * L + (L - k)) * D + ch] = f2bf(c + sn + as);
.LBB0_848:
	s_or_b64 exec, exec, s[66:67]
	v_add_u32_e32 v14, 48, v62
	v_ashrrev_i32_e32 v15, 31, v14
	v_lshlrev_b64 v[16:17], 13, v[14:15]
	v_lshl_add_u64 v[16:17], s[64:65], 0, v[16:17]
	v_mov_b32_e32 v16, v232
	v_sub_f32_e32 v17, v42, v50
	v_lshl_add_u64 v[14:15], v[14:15], 1, s[16:17]
	v_lshl_add_u64 v[32:33], v[14:15], 0, v[74:75]
	v_lshlrev_b32_e32 v16, 16, v16
	v_add_f32_e32 v17, v17, v16
	v_cvt_pk_bf16_f32 v17, v17, s0
	global_store_short v[32:33], v17, off
	s_and_saveexec_b64 s[66:67], s[6:7]
	s_cbranch_execz .LBB0_850
	v_add_f32_e32 v17, v42, v50
	v_lshl_add_u64 v[32:33], s[62:63], 0, v[48:49]
	v_add_f32_e32 v17, v17, v16
	v_lshlrev_b64 v[32:33], 12, v[32:33]
	v_cvt_pk_bf16_f32 v17, v17, s0
	v_lshl_add_u64 v[32:33], v[14:15], 0, v[32:33]
	global_store_short v[32:33], v17, off

; __device__ __forceinline__ float bf2f(bf16_t h) { return __uint_as_float(((uint32_t)h) << 16); }
; __device__ void phase_ssd_dft(KParams& p, int bid, int nb, char* smem) {
;     ...
;         const int k0 = tm * 128 + wm * 64 + i * 16 + lq_ * 4;
;         const int ch = tn * 128 + wn * 64 + j * 16 + lr_;
;         const float a = bf2f(p.ABt[((size_t)b * 1024 + ch) * 4096 + 1024]);
; #pragma unroll
;         for (int r = 0; r < 4; ++r) {
;           const int k = k0 + r;
;           const float as = (k & 1) ? -a : a;
;           const float c = accC[i][j][r], sn = accS[i][j][r];
;           p.ycat[((size_t)b * L + k) * D + ch] = f2bf(c - sn + as);
;           if (k > 0) p.ycat[((size_t)b * L + (L - k)) * D + ch] = f2bf(c + sn + as);
.LBB0_856:
	s_or_b64 exec, exec, s[6:7]
	v_mov_b32_e32 v16, v195
	v_mov_b32_e32 v14, v185
	v_sub_f32_e32 v44, v6, v38
	v_add_u32_e32 v30, v14, v142
	v_ashrrev_i32_e32 v31, 31, v30
	v_lshlrev_b64 v[14:15], 13, v[30:31]
	v_lshl_add_u64 v[14:15], s[64:65], 0, v[14:15]
	v_mov_b32_e32 v17, v229
	v_lshlrev_b32_e32 v14, 2, v16
	v_add3_u32 v32, v14, v143, 48
	v_ashrrev_i32_e32 v33, 31, v32
	v_lshl_add_u64 v[48:49], v[30:31], 1, s[16:17]
	v_lshl_add_u64 v[14:15], s[62:63], 0, v[32:33]
	v_lshlrev_b64 v[42:43], 12, v[14:15]
	v_sub_u32_e32 v16, 0x800, v32
	v_lshl_add_u64 v[14:15], v[48:49], 0, v[42:43]
	v_cmp_lt_i32_e64 s[6:7], 0, v32
	v_lshlrev_b32_e32 v31, 16, v17
	v_add_f32_e32 v17, v44, v31
	v_cvt_pk_bf16_f32 v17, v17, s0
	global_store_short v[14:15], v17, off
	v_ashrrev_i32_e32 v17, 31, v16
	s_and_saveexec_b64 s[8:9], s[6:7]
	s_cbranch_execz .LBB0_858
	v_add_f32_e32 v6, v6, v38
	v_lshl_add_u64 v[14:15], s[62:63], 0, v[16:17]
	v_add_f32_e32 v6, v6, v31
	v_lshlrev_b64 v[14:15], 12, v[14:15]
	v_cvt_pk_bf16_f32 v6, v6, s0
	v_lshl_add_u64 v[14:15], v[48:49], 0, v[14:15]
	global_store_short v[14:15], v6, off

; __device__ __forceinline__ float bf2f(bf16_t h) { return __uint_as_float(((uint32_t)h) << 16); }
; __device__ void phase_ssd_dft(KParams& p, int bid, int nb, char* smem) {
;     ...
;         const int k0 = tm * 128 + wm * 64 + i * 16 + lq_ * 4;
;         const int ch = tn * 128 + wn * 64 + j * 16 + lr_;
;         const float a = bf2f(p.ABt[((size_t)b * 1024 + ch) * 4096 + 1024]);
; #pragma unroll
;         for (int r = 0; r < 4; ++r) {
;           const int k = k0 + r;
;           const float as = (k & 1) ? -a : a;
;           const float c = accC[i][j][r], sn = accS[i][j][r];
;           p.ycat[((size_t)b * L + k) * D + ch] = f2bf(c - sn + as);
;           if (k > 0) p.ycat[((size_t)b * L + (L - k)) * D + ch] = f2bf(c + sn + as);
.LBB0_864:
	s_or_b64 exec, exec, s[66:67]
	v_add_u32_e32 v8, 16, v30
	v_ashrrev_i32_e32 v9, 31, v8
	v_lshlrev_b64 v[40:41], 13, v[8:9]
	v_lshl_add_u64 v[40:41], s[64:65], 0, v[40:41]
	v_mov_b32_e32 v31, v230
	v_sub_f32_e32 v40, v22, v34
	v_lshl_add_u64 v[8:9], v[8:9], 1, s[16:17]
	v_lshlrev_b32_e32 v31, 16, v31
	v_add_f32_e32 v40, v40, v31
	v_cvt_pk_bf16_f32 v48, v40, s0
	v_lshl_add_u64 v[40:41], v[8:9], 0, v[42:43]
	global_store_short v[40:41], v48, off
	s_and_saveexec_b64 s[66:67], s[6:7]
	s_cbranch_execz .LBB0_866
	v_add_f32_e32 v22, v22, v34
	v_lshl_add_u64 v[40:41], s[62:63], 0, v[16:17]
	v_add_f32_e32 v22, v22, v31
	v_lshlrev_b64 v[40:41], 12, v[40:41]
	v_cvt_pk_bf16_f32 v22, v22, s0
	v_lshl_add_u64 v[40:41], v[8:9], 0, v[40:41]
	global_store_short v[40:41], v22, off

; __device__ __forceinline__ float bf2f(bf16_t h) { return __uint_as_float(((uint32_t)h) << 16); }
; __device__ void phase_ssd_dft(KParams& p, int bid, int nb, char* smem) {
;     ...
;         const int k0 = tm * 128 + wm * 64 + i * 16 + lq_ * 4;
;         const int ch = tn * 128 + wn * 64 + j * 16 + lr_;
;         const float a = bf2f(p.ABt[((size_t)b * 1024 + ch) * 4096 + 1024]);
; #pragma unroll
;         for (int r = 0; r < 4; ++r) {
;           const int k = k0 + r;
;           const float as = (k & 1) ? -a : a;
;           const float c = accC[i][j][r], sn = accS[i][j][r];
;           p.ycat[((size_t)b * L + k) * D + ch] = f2bf(c - sn + as);
;           if (k > 0) p.ycat[((size_t)b * L + (L - k)) * D + ch] = f2bf(c + sn + as);
.LBB0_870:
	s_or_b64 exec, exec, s[66:67]
	v_add_u32_e32 v8, 32, v30
	v_ashrrev_i32_e32 v9, 31, v8
	v_lshlrev_b64 v[22:23], 13, v[8:9]
	v_lshl_add_u64 v[22:23], s[64:65], 0, v[22:23]
	v_mov_b32_e32 v22, v231
	v_sub_f32_e32 v23, v2, v26
	v_lshl_add_u64 v[8:9], v[8:9], 1, s[16:17]
	v_lshlrev_b32_e32 v24, 16, v22
	v_add_f32_e32 v22, v23, v24
	v_cvt_pk_bf16_f32 v25, v22, s0
	v_lshl_add_u64 v[22:23], v[8:9], 0, v[42:43]
	global_store_short v[22:23], v25, off
	s_and_saveexec_b64 s[66:67], s[6:7]
	s_cbranch_execz .LBB0_872
	v_add_f32_e32 v2, v2, v26
	v_lshl_add_u64 v[22:23], s[62:63], 0, v[16:17]
	v_add_f32_e32 v2, v2, v24
	v_lshlrev_b64 v[22:23], 12, v[22:23]
	v_cvt_pk_bf16_f32 v2, v2, s0
	v_lshl_add_u64 v[22:23], v[8:9], 0, v[22:23]
	global_store_short v[22:23], v2, off

; __device__ __forceinline__ float bf2f(bf16_t h) { return __uint_as_float(((uint32_t)h) << 16); }
; __device__ void phase_ssd_dft(KParams& p, int bid, int nb, char* smem) {
;     ...
;         const int k0 = tm * 128 + wm * 64 + i * 16 + lq_ * 4;
;         const int ch = tn * 128 + wn * 64 + j * 16 + lr_;
;         const float a = bf2f(p.ABt[((size_t)b * 1024 + ch) * 4096 + 1024]);
; #pragma unroll
;         for (int r = 0; r < 4; ++r) {
;           const int k = k0 + r;
;           const float as = (k & 1) ? -a : a;
;           const float c = accC[i][j][r], sn = accS[i][j][r];
;           p.ycat[((size_t)b * L + k) * D + ch] = f2bf(c - sn + as);
;           if (k > 0) p.ycat[((size_t)b * L + (L - k)) * D + ch] = f2bf(c + sn + as);
.LBB0_876:
	s_or_b64 exec, exec, s[66:67]
	v_add_u32_e32 v2, 48, v30
	v_ashrrev_i32_e32 v3, 31, v2
	v_lshlrev_b64 v[4:5], 13, v[2:3]
	v_lshl_add_u64 v[4:5], s[64:65], 0, v[4:5]
	v_mov_b32_e32 v4, v232
	v_sub_f32_e32 v5, v10, v18
	v_lshl_add_u64 v[2:3], v[2:3], 1, s[16:17]
	v_lshl_add_u64 v[8:9], v[2:3], 0, v[42:43]
	v_lshlrev_b32_e32 v4, 16, v4
	v_add_f32_e32 v5, v5, v4
	v_cvt_pk_bf16_f32 v5, v5, s0
	global_store_short v[8:9], v5, off
	s_and_saveexec_b64 s[64:65], s[6:7]
	s_cbranch_execz .LBB0_878
	v_add_f32_e32 v5, v10, v18
	v_lshl_add_u64 v[8:9], s[62:63], 0, v[16:17]
	v_add_f32_e32 v5, v5, v4
	v_lshlrev_b64 v[8:9], 12, v[8:9]
	v_cvt_pk_bf16_f32 v5, v5, s0
	v_lshl_add_u64 v[8:9], v[2:3], 0, v[8:9]
	global_store_short v[8:9], v5, off
